# HGRN2 chunk loop: the two output stores of a chunk are held in registers and issued after the next trip's loads, so the loads no longer retire behind the store acknowledgements (plus 32-bit saddr row
# baseline (speedup 1.0000x reference)
; __device__ __forceinline__ void hgrn_mfma(const Params& p, LAS unsigned char* lds) {
;     ...
;         const int b = u >> 4, h = (u >> 1) & 7, dir = u & 1;
;         const int d = 16 * w + fr;
;         float lb; { const float l0 = lbl[h * 128 + d], l1 = lbl[1024 + h * 128 + d], l2 = lbl[2048 + h * 128 + d];
;             const float mx = fmaxf(l0, fmaxf(l1, l2)); const float e0 = expf(l0 - mx), e1 = expf(l1 - mx), e2 = expf(l2 - mx); lb = e0 / (e0 + e1 + e2); }
;         f32x4 S[8];
; #pragma unroll
;         for (int mi = 0; mi < 8; ++mi) S[mi] = (f32x4){0.f, 0.f, 0.f, 0.f};
;         const bf16_t* pb = proj + (size_t)b * T * LD0 + h * 128 + d;
;         const int zoff = dir ? 3072 : 2048;
;         bf16_t rq[8], rz[8], rv[8], rp[8];
;     ...
;         HG_LOAD(0);
.LBB0_274:
	s_lshl_b32 s18, s53, 6
	s_and_b32 s18, s18, 0x380
	v_add_u32_e32 v2, s18, v38
	v_ashrrev_i32_e32 v3, 31, v2
	s_waitcnt lgkmcnt(0)
	v_lshl_add_u64 v[2:3], v[2:3], 2, s[40:41]
	v_add_co_u32_e32 v6, vcc, 0x1000, v2
	s_ashr_i32 s46, s53, 4
	s_nop 0
	v_addc_co_u32_e32 v7, vcc, 0, v3, vcc
	v_add_co_u32_e32 v8, vcc, 0x2000, v2
	s_and_b32 s54, s53, 1
	s_nop 0
	v_addc_co_u32_e32 v9, vcc, 0, v3, vcc
	global_load_dword v0, v[2:3], off
	global_load_dword v16, v[6:7], off
	global_load_dword v17, v[8:9], off
	s_ashr_i32 s47, s46, 31
	s_mul_i32 s42, s46, 0x2040000
	s_mul_hi_i32 s19, s46, 0x2040000
	s_add_u32 s42, s36, s42
	s_addc_u32 s19, s37, s19
	s_lshl_b32 s56, s18, 1
	s_add_u32 s18, s42, s56
	s_addc_u32 s19, s19, 0
	s_cmp_eq_u32 s54, 0
	v_lshl_add_u64 v[44:45], v[38:39], 1, s[18:19]
	s_cselect_b64 s[18:19], -1, 0
	v_cndmask_b32_e64 v2, v66, v41, s[18:19]
	v_cndmask_b32_e64 v5, v67, v40, s[18:19]
	v_cndmask_b32_e64 v8, v69, v68, s[18:19]
	s_and_b64 s[58:59], s[18:19], exec
	v_mul_u32_u24_e32 v2, 0x2040, v2
	v_mul_u32_u24_e32 v6, 0x4080, v5
	v_mul_u32_u24_e32 v5, 0x2040, v8
	v_mov_b32_e32 v3, v4
	v_mov_b32_e32 v9, v4
	v_cndmask_b32_e64 v10, v71, v70, s[18:19]
	s_cselect_b32 s55, s50, 0xc00
	v_lshlrev_b32_e32 v2, 1, v2
	v_lshlrev_b32_e32 v8, 1, v5
	v_mov_b32_e32 v7, v4
	v_mov_b32_e32 v11, v4
	v_mul_u32_u24_e32 v10, 0x4080, v10
	v_lshl_add_u64 v[2:3], v[44:45], 0, v[2:3]
	s_lshl_b32 s42, s55, 1
	v_lshl_add_u64 v[8:9], v[44:45], 0, v[8:9]
	v_lshl_add_u64 v[6:7], v[44:45], 0, v[6:7]
	v_lshl_add_u64 v[10:11], v[44:45], 0, v[10:11]
	v_lshl_add_u64 v[12:13], v[2:3], 0, s[42:43]
	v_lshl_add_u64 v[14:15], v[8:9], 0, s[42:43]
	global_load_ushort v135, v[2:3], off
	global_load_ushort v159, v[2:3], off offset:2048
	global_load_ushort v137, v[12:13], off
	global_load_ushort v171, v[6:7], off offset:2048
	global_load_ushort v136, v[8:9], off
	global_load_ushort v160, v[8:9], off offset:2048
	global_load_ushort v138, v[14:15], off
	global_load_ushort v5, v[10:11], off offset:2048
	v_cndmask_b32_e64 v18, v73, v72, s[18:19]
	v_cndmask_b32_e64 v14, v79, v78, s[18:19]
	v_mul_u32_u24_e32 v14, 0x4080, v14
	v_mov_b32_e32 v15, v4
	v_lshl_add_u64 v[14:15], v[44:45], 0, v[14:15]
	s_lshl_b64 s[46:47], s[46:47], 22
	v_mov_b32_e32 v21, v4
	v_mov_b32_e32 v22, v4
	v_mov_b32_e32 v23, v4
	v_mov_b32_e32 v24, v4
	v_mov_b32_e32 v25, v4
	v_mov_b32_e32 v26, v4
	v_mov_b32_e32 v27, v4
	v_mov_b32_e32 v28, v4
	v_mov_b32_e32 v29, v4
	v_mov_b32_e32 v30, v4
	v_mov_b32_e32 v31, v4
	v_mov_b32_e32 v32, v4
	v_mov_b32_e32 v33, v4
	v_mov_b32_e32 v34, v4
	v_mov_b32_e32 v35, v4
	v_mov_b32_e32 v36, v4
	v_mov_b32_e32 v37, v4
	s_waitcnt vmcnt(8)
	v_max3_f32 v2, v0, v16, v17
	v_sub_f32_e32 v0, v0, v2
	v_sub_f32_e32 v3, v16, v2
	v_sub_f32_e32 v16, v17, v2
	v_mul_f32_e32 v2, 0x3fb8aa3b, v0
	v_mul_f32_e32 v6, 0x3fb8aa3b, v3
	v_fma_f32 v8, v0, s3, -v2
	v_rndne_f32_e32 v9, v2
	v_fma_f32 v10, v3, s3, -v6
	v_rndne_f32_e32 v11, v6
	v_fmac_f32_e32 v8, 0x32a5705f, v0
	v_sub_f32_e32 v2, v2, v9
	v_fmac_f32_e32 v10, 0x32a5705f, v3
	v_sub_f32_e32 v6, v6, v11
	v_add_f32_e32 v2, v2, v8
	v_cvt_i32_f32_e32 v9, v9
	v_add_f32_e32 v6, v6, v10
	v_exp_f32_e32 v2, v2
	v_cvt_i32_f32_e32 v11, v11
	v_exp_f32_e32 v6, v6
	v_cmp_ngt_f32_e32 vcc, s48, v0
	v_ldexp_f32 v2, v2, v9
	v_mul_f32_e32 v7, 0x3fb8aa3b, v16
	v_ldexp_f32 v6, v6, v11
	v_cndmask_b32_e32 v2, 0, v2, vcc
	v_cmp_ngt_f32_e32 vcc, s48, v3
	v_cndmask_b32_e64 v10, v77, v76, s[18:19]
	v_fma_f32 v12, v16, s3, -v7
	v_cndmask_b32_e32 v6, 0, v6, vcc
	v_cmp_nlt_f32_e32 vcc, s49, v0
	v_rndne_f32_e32 v13, v7
	v_mul_u32_u24_e32 v10, 0x2040, v10
	v_cndmask_b32_e32 v0, v134, v2, vcc
	v_mul_u32_u24_e32 v2, 0x2040, v18
	v_fmac_f32_e32 v12, 0x32a5705f, v16
	v_sub_f32_e32 v7, v7, v13
	v_cmp_nlt_f32_e32 vcc, s49, v3
	v_lshlrev_b32_e32 v2, 1, v2
	v_mov_b32_e32 v3, v4
	v_cndmask_b32_e64 v8, v75, v74, s[18:19]
	v_lshlrev_b32_e32 v10, 1, v10
	v_mov_b32_e32 v11, v4
	v_add_f32_e32 v7, v7, v12
	v_lshl_add_u64 v[2:3], v[44:45], 0, v[2:3]
	v_mul_u32_u24_e32 v8, 0x4080, v8
	v_mov_b32_e32 v9, v4
	v_lshl_add_u64 v[10:11], v[44:45], 0, v[10:11]
	v_cvt_i32_f32_e32 v17, v13
	v_exp_f32_e32 v19, v7
	v_cndmask_b32_e32 v20, v134, v6, vcc
	v_lshl_add_u64 v[6:7], v[2:3], 0, s[42:43]
	v_lshl_add_u64 v[8:9], v[44:45], 0, v[8:9]
	v_lshl_add_u64 v[12:13], v[10:11], 0, s[42:43]
	global_load_ushort v139, v[2:3], off
	global_load_ushort v165, v[2:3], off offset:2048
	global_load_ushort v141, v[6:7], off
	global_load_ushort v175, v[8:9], off offset:2048
	global_load_ushort v144, v[10:11], off
	global_load_ushort v161, v[10:11], off offset:2048
	global_load_ushort v145, v[12:13], off
	global_load_ushort v172, v[14:15], off offset:2048
	v_cndmask_b32_e64 v2, v81, v80, s[18:19]
	v_cndmask_b32_e64 v10, v85, v84, s[18:19]
	v_mul_u32_u24_e32 v2, 0x2040, v2
	v_mul_u32_u24_e32 v10, 0x2040, v10
	v_lshlrev_b32_e32 v2, 1, v2
	v_mov_b32_e32 v3, v4
	v_cndmask_b32_e64 v8, v83, v82, s[18:19]
	v_lshlrev_b32_e32 v10, 1, v10
	v_mov_b32_e32 v11, v4
	v_cndmask_b32_e64 v14, v87, v86, s[18:19]
	v_lshl_add_u64 v[2:3], v[44:45], 0, v[2:3]
	v_mul_u32_u24_e32 v8, 0x4080, v8
	v_mov_b32_e32 v9, v4
	v_lshl_add_u64 v[10:11], v[44:45], 0, v[10:11]
	v_mul_u32_u24_e32 v14, 0x4080, v14
	v_mov_b32_e32 v15, v4
	v_lshl_add_u64 v[6:7], v[2:3], 0, s[42:43]
	v_lshl_add_u64 v[8:9], v[44:45], 0, v[8:9]
	v_lshl_add_u64 v[12:13], v[10:11], 0, s[42:43]
	v_lshl_add_u64 v[14:15], v[44:45], 0, v[14:15]
	global_load_ushort v149, v[2:3], off
	global_load_ushort v163, v[2:3], off offset:2048
	global_load_ushort v151, v[6:7], off
	global_load_ushort v177, v[8:9], off offset:2048
	global_load_ushort v153, v[10:11], off
	global_load_ushort v166, v[10:11], off offset:2048
; #define LAS __attribute__((address_space(3)))
; __device__ __forceinline__ float bf2f(bf16_t v) { return __uint_as_float((unsigned)v << 16); }
; __device__ __forceinline__ float sigm(float x) { return frcp(1.f + __expf(-x)); }
; __device__ __forceinline__ void hgrn_mfma(const Params& p, LAS unsigned char* lds) {
;     ...
;         const bf16_t* pb = proj + (size_t)b * T * LD0 + h * 128 + d;
;         const int zoff = dir ? 3072 : 2048;
;         bf16_t rq[8], rz[8], rv[8], rp[8];
;     ...
;         HG_LOAD(0);
;         for (int n = 0; n < T / 32; ++n) {
;             LAS unsigned char* set = lds + (n & 1) * SET_BYTES;
;             LAS unsigned char* QG = set; LAS unsigned char* KG = set + 8192; LAS unsigned char* KDT = set + 16384; LAS float* DEC = (LAS float*)(set + 24576);
;             float qv[8], fv[8], vv[8], vp[8];
; #pragma unroll
;             for (int i = 0; i < 8; ++i) { qv[i] = bf2f(rq[i]); vv[i] = bf2f(rv[i]); fv[i] = bf2f(rz[i]); vp[i] = bf2f(rp[i]); }
;             if (n + 1 < T / 32) HG_LOAD(n + 1);
;             float Pl[8]; float P = 1.f;
; #pragma unroll
;             for (int i = 0; i < 8; ++i) { fv[i] = lb + (1.f - lb) * sigm(fv[i]); P *= fv[i]; Pl[i] = P; }
	global_load_ushort v154, v[12:13], off
	global_load_ushort v176, v[14:15], off offset:2048
	v_cndmask_b32_e64 v2, v89, v88, s[18:19]
	v_cndmask_b32_e64 v10, v93, v92, s[18:19]
	v_mul_u32_u24_e32 v2, 0x2040, v2
	v_mul_u32_u24_e32 v10, 0x2040, v10
	v_lshlrev_b32_e32 v2, 1, v2
	v_mov_b32_e32 v3, v4
	v_cndmask_b32_e64 v8, v91, v90, s[18:19]
	v_lshlrev_b32_e32 v10, 1, v10
	v_mov_b32_e32 v11, v4
	v_cndmask_b32_e64 v14, v95, v94, s[18:19]
	v_lshl_add_u64 v[2:3], v[44:45], 0, v[2:3]
	v_mul_u32_u24_e32 v8, 0x4080, v8
	v_mov_b32_e32 v9, v4
	v_lshl_add_u64 v[10:11], v[44:45], 0, v[10:11]
	v_mul_u32_u24_e32 v14, 0x4080, v14
	v_mov_b32_e32 v15, v4
	v_lshl_add_u64 v[6:7], v[2:3], 0, s[42:43]
	v_lshl_add_u64 v[8:9], v[44:45], 0, v[8:9]
	v_lshl_add_u64 v[12:13], v[10:11], 0, s[42:43]
	v_lshl_add_u64 v[14:15], v[44:45], 0, v[14:15]
	global_load_ushort v155, v[2:3], off
	global_load_ushort v162, v[2:3], off offset:2048
	global_load_ushort v156, v[6:7], off
	global_load_ushort v180, v[8:9], off offset:2048
	global_load_ushort v157, v[10:11], off
	global_load_ushort v164, v[10:11], off offset:2048
	global_load_ushort v158, v[12:13], off
	global_load_ushort v181, v[14:15], off offset:2048
	v_ldexp_f32 v2, v19, v17
	v_cmp_ngt_f32_e32 vcc, s48, v16
	v_add_f32_e32 v3, v0, v20
	s_add_u32 s42, s38, s46
	v_cndmask_b32_e32 v2, 0, v2, vcc
	v_cmp_nlt_f32_e32 vcc, s49, v16
	s_addc_u32 s46, s39, s47
	s_lshl_b32 s47, s54, 25
	v_cndmask_b32_e32 v2, v134, v2, vcc
	v_add_f32_e32 v2, v2, v3
	v_div_scale_f32 v3, s[58:59], v2, v2, v0
	v_rcp_f32_e32 v6, v3
	s_add_u32 s42, s42, s47
	s_addc_u32 s46, s46, 0
	s_add_u32 s42, s42, s56
	v_fma_f32 v7, -v3, v6, 1.0
	v_fmac_f32_e32 v6, v7, v6
	v_div_scale_f32 v7, vcc, v0, v2, v0
	v_mul_f32_e32 v8, v7, v6
	v_fma_f32 v9, -v3, v8, v7
	v_fmac_f32_e32 v8, v9, v6
	v_fma_f32 v3, -v3, v8, v7
	v_div_fmas_f32 v3, v3, v6, v8
	s_addc_u32 s47, s46, 0
	v_div_fixup_f32 v50, v3, v2, v0
	s_add_u32 s46, s42, s44
	v_sub_f32_e32 v52, 1.0, v50
	s_addc_u32 s47, s47, s45
	v_lshlrev_b32_e32 v2, 1, v40
	v_mov_b32_e32 v3, v4
	v_lshl_add_u64 v[42:43], s[46:47], 0, v[2:3]
	v_mov_b32_e32 v54, v50
	v_mov_b32_e32 v46, v50
	v_mov_b32_e32 v47, v50
	v_mov_b32_e32 v48, v52
	v_mov_b32_e32 v49, v52
	s_lshl_b32 s42, s55, 1
	s_mov_b32 s54, s43
	s_mov_b32 s55, s43
	s_mov_b32 s56, s43
	v_mov_b32_e32 v14, v4
	v_mov_b32_e32 v15, v4
	v_mov_b32_e32 v16, v4
	v_mov_b32_e32 v17, v4
	v_mov_b32_e32 v6, v4
	v_mov_b32_e32 v7, v4
	v_mov_b32_e32 v8, v4
	v_mov_b32_e32 v9, v4
	v_mov_b32_e32 v10, v4
	v_mov_b32_e32 v11, v4
	v_mov_b32_e32 v12, v4
	v_mov_b32_e32 v13, v4
	v_mov_b32_e32 v18, v4
	v_mov_b32_e32 v19, v4
	v_mov_b32_e32 v20, v4
	v_readfirstlane_b32 s80, v44
	v_readfirstlane_b32 s81, v45
	s_mov_b32 s84, 0x81000
	s_mov_b32 s85, 0x4080
	s_mov_b32 s86, 0x40800
	s_cmp_lg_u64 s[18:19], 0
	s_cselect_b32 s84, s84, 0xfff7f000
	s_cselect_b32 s85, s85, 0xffffbf80
	s_cselect_b32 s86, s86, 0xfffbf800
	s_nop 1
	s_add_u32 s82, s80, s42
	s_addc_u32 s83, s81, s43
	v_subrev_u32_e32 v132, s80, v44
	v_add_u32_e32 v250, 32, v41
	v_sub_u32_e32 v251, 0x7df, v41
	v_cndmask_b32_e64 v250, v251, v250, s[18:19]
	v_mul_u32_u24_e32 v250, 0x4080, v250
	v_add_u32_e32 v232, v250, v132
	v_add_u32_e32 v233, s85, v232
	v_add_u32_e32 v234, s85, v233
	v_add_u32_e32 v235, s85, v234
	v_add_u32_e32 v236, s85, v235
	v_add_u32_e32 v237, s85, v236
	v_add_u32_e32 v238, s85, v237
	v_add_u32_e32 v239, s85, v238
	v_add_u32_e32 v252, 32, v40
	v_sub_u32_e32 v253, 0x7df, v40
	v_cndmask_b32_e64 v252, v253, v252, s[18:19]
	v_mul_u32_u24_e32 v252, 0x4080, v252
	v_add_u32_e32 v240, v252, v132
	v_add_u32_e32 v242, s85, v240
	v_add_u32_e32 v243, s85, v242
	v_add_u32_e32 v244, s85, v243
	v_add_u32_e32 v245, s86, v240
	v_add_u32_e32 v246, s85, v245
	v_add_u32_e32 v247, s85, v246
	v_add_u32_e32 v254, s85, v247
	s_nop 3
	v_mov_b64_e32 v[248:249], v[42:43]
	v_mov_b64_e32 v[252:253], v[42:43]
	v_mov_b32_e32 v250, 0
	v_mov_b32_e32 v251, 0
	v_mov_b32_e32 v132, 0
	v_mov_b32_e32 v133, 0
.LBB0_275:
	s_bitcmp1_b32 s56, 0
	s_waitcnt vmcnt(31)
	v_lshlrev_b32_e32 v0, 16, v135
	s_waitcnt vmcnt(25)
	v_lshlrev_b32_e32 v53, 16, v138
	s_waitcnt vmcnt(1)
	v_lshlrev_b32_e32 v199, 16, v158
	s_cselect_b32 s46, 0x6200, 0
	s_add_i32 s57, s46, 0
	v_lshlrev_b32_e32 v193, 16, v139
	v_lshlrev_b32_e32 v55, 16, v141
	v_lshlrev_b32_e32 v51, 16, v137
	v_lshlrev_b32_e32 v192, 16, v136
	v_lshlrev_b32_e32 v194, 16, v144
	v_lshlrev_b32_e32 v195, 16, v145
	global_load_ushort v135, v232, s[80:81]
	global_load_ushort v167, v232, s[80:81] offset:2048
	s_nop 0
	global_load_ushort v137, v232, s[82:83]
	s_nop 0
	global_load_ushort v143, v240, s[80:81] offset:2048
	global_load_ushort v136, v233, s[80:81]
	global_load_ushort v168, v233, s[80:81] offset:2048
	s_nop 0
	global_load_ushort v138, v233, s[82:83]
	global_load_ushort v140, v242, s[80:81] offset:2048
	v_lshlrev_b32_e32 v204, 16, v149
	v_lshlrev_b32_e32 v196, 16, v151
	v_lshlrev_b32_e32 v205, 16, v153
	global_load_ushort v139, v234, s[80:81]
	global_load_ushort v169, v234, s[80:81] offset:2048
	global_load_ushort v141, v234, s[82:83]
	s_nop 0
	global_load_ushort v146, v243, s[80:81] offset:2048
	s_nop 0
	global_load_ushort v144, v235, s[80:81]
	global_load_ushort v170, v235, s[80:81] offset:2048
	global_load_ushort v145, v235, s[82:83]
	global_load_ushort v142, v244, s[80:81] offset:2048
	v_mul_f32_e32 v51, 0xbfb8aa3b, v51
	v_exp_f32_e32 v51, v51
	v_mul_f32_e32 v53, 0xbfb8aa3b, v53
	v_lshlrev_b32_e32 v197, 16, v154
	v_lshlrev_b32_e32 v206, 16, v155
	v_exp_f32_e32 v53, v53
	v_lshlrev_b32_e32 v198, 16, v156
	v_lshlrev_b32_e32 v207, 16, v157
	global_load_ushort v149, v236, s[80:81]
	global_load_ushort v173, v236, s[80:81] offset:2048
; #define LAS __attribute__((address_space(3)))
; __device__ __forceinline__ float bf2f(bf16_t v) { return __uint_as_float((unsigned)v << 16); }
; __device__ __forceinline__ float sigm(float x) { return frcp(1.f + __expf(-x)); }
; __device__ __forceinline__ void hgrn_mfma(const Params& p, LAS unsigned char* lds) {
;     ...
;         HG_LOAD(0);
;         for (int n = 0; n < T / 32; ++n) {
;             LAS unsigned char* set = lds + (n & 1) * SET_BYTES;
;             LAS unsigned char* QG = set; LAS unsigned char* KG = set + 8192; LAS unsigned char* KDT = set + 16384; LAS float* DEC = (LAS float*)(set + 24576);
;             float qv[8], fv[8], vv[8], vp[8];
; #pragma unroll
;             for (int i = 0; i < 8; ++i) { qv[i] = bf2f(rq[i]); vv[i] = bf2f(rv[i]); fv[i] = bf2f(rz[i]); vp[i] = bf2f(rp[i]); }
;             if (n + 1 < T / 32) HG_LOAD(n + 1);
;             float Pl[8]; float P = 1.f;
; #pragma unroll
;             for (int i = 0; i < 8; ++i) { fv[i] = lb + (1.f - lb) * sigm(fv[i]); P *= fv[i]; Pl[i] = P; }
;             const float p0 = __shfl(P, fr), p1 = __shfl(P, fr + 16), p2 = __shfl(P, fr + 32), p3 = __shfl(P, fr + 48);
	s_nop 0
	global_load_ushort v151, v236, s[82:83]
	s_nop 0
	global_load_ushort v147, v245, s[80:81] offset:2048
	s_nop 0
	global_load_ushort v153, v237, s[80:81]
	global_load_ushort v174, v237, s[80:81] offset:2048
	s_nop 0
	global_load_ushort v154, v237, s[82:83]
	global_load_ushort v148, v246, s[80:81] offset:2048
	v_add_f32_e32 v51, 1.0, v51
	v_rcp_f32_e32 v191, v51
	v_add_f32_e32 v51, 1.0, v53
	v_rcp_f32_e32 v190, v51
	v_mul_f32_e32 v51, 0xbfb8aa3b, v196
	v_exp_f32_e32 v51, v51
	global_load_ushort v155, v238, s[80:81]
	global_load_ushort v178, v238, s[80:81] offset:2048
	s_nop 0
	global_load_ushort v156, v238, s[82:83]
	s_nop 0
	global_load_ushort v150, v247, s[80:81] offset:2048
	global_load_ushort v157, v239, s[80:81]
	global_load_ushort v179, v239, s[80:81] offset:2048
	global_load_ushort v158, v239, s[82:83]
	global_load_ushort v152, v254, s[80:81] offset:2048
	v_add_u32_e32 v232, s84, v232
	v_add_u32_e32 v233, s84, v233
	v_add_u32_e32 v234, s84, v234
	v_add_u32_e32 v235, s84, v235
	v_add_u32_e32 v236, s84, v236
	v_add_u32_e32 v237, s84, v237
	v_add_u32_e32 v238, s84, v238
	v_add_u32_e32 v239, s84, v239
	v_add_u32_e32 v240, s84, v240
	v_add_u32_e32 v242, s84, v242
	v_add_u32_e32 v243, s84, v243
	v_add_u32_e32 v244, s84, v244
	v_add_u32_e32 v245, s84, v245
	v_add_u32_e32 v246, s84, v246
	v_add_u32_e32 v247, s84, v247
	v_add_u32_e32 v254, s84, v254
	global_store_dwordx2 v[248:249], v[250:251], off
	global_store_dwordx2 v[252:253], v[132:133], off
	v_mul_f32_e32 v188, 0xbfb8aa3b, v192
	v_add_f32_e32 v51, 1.0, v51
	v_exp_f32_e32 v188, v188
	v_rcp_f32_e32 v186, v51
	v_mul_f32_e32 v51, 0xbfb8aa3b, v199
	v_exp_f32_e32 v51, v51
	v_add_f32_e32 v188, 1.0, v188
	v_rcp_f32_e32 v189, v188
	v_mul_f32_e32 v2, 0xbfb8aa3b, v55
	v_add_f32_e32 v51, 1.0, v51
	v_mul_f32_e32 v3, 0xbfb8aa3b, v195
	v_rcp_f32_e32 v188, v51
	v_mul_f32_e32 v51, 0xbfb8aa3b, v193
	v_exp_f32_e32 v2, v2
	v_exp_f32_e32 v3, v3
	v_exp_f32_e32 v51, v51
	v_mul_f32_e32 v208, v189, v192
	v_mul_f32_e32 v189, 0xbfb8aa3b, v194
	v_exp_f32_e32 v189, v189
	v_add_f32_e32 v2, 1.0, v2
	v_add_f32_e32 v3, 1.0, v3
	v_add_f32_e32 v51, 1.0, v51
	v_rcp_f32_e32 v2, v2
	v_rcp_f32_e32 v3, v3
	v_mul_f32_e32 v53, 0xbfb8aa3b, v197
	v_rcp_f32_e32 v51, v51
	v_exp_f32_e32 v53, v53
	v_mul_f32_e32 v55, 0xbfb8aa3b, v198
	v_add_f32_e32 v189, 1.0, v189
	v_exp_f32_e32 v55, v55
	v_rcp_f32_e32 v189, v189
	v_pk_fma_f32 v[182:183], v[48:49], v[190:191], v[46:47]
	v_mul_f32_e32 v210, v51, v193
	v_pk_mul_f32 v[184:185], v[182:183], v[182:183] op_sel:[0,1] op_sel_hi:[1,0]
	v_pk_fma_f32 v[192:193], v[48:49], v[2:3], v[46:47]
	v_add_f32_e32 v53, 1.0, v53
	v_mov_b32_e32 v187, v184
	v_mov_b32_e32 v2, v52
	v_mov_b32_e32 v3, v192
	v_rcp_f32_e32 v53, v53
	v_add_f32_e32 v55, 1.0, v55
	v_mul_f32_e32 v212, v189, v194
	v_pk_mul_f32 v[194:195], v[2:3], v[186:187]
	v_mov_b32_e32 v51, v193
	v_rcp_f32_e32 v55, v55
	v_pk_fma_f32 v[186:187], v[2:3], v[186:187], v[50:51]
	v_pk_mul_f32 v[196:197], v[50:51], v[194:195]
	v_fma_f32 v53, v52, v53, v50
	v_mov_b32_e32 v187, v197
	v_pk_mul_f32 v[198:199], v[186:187], v[196:197] op_sel:[0,1] op_sel_hi:[1,0]
	v_fma_f32 v55, v52, v55, v50
	v_mov_b32_e32 v189, v198
	v_pk_mul_f32 v[200:201], v[52:53], v[188:189]
	v_mul_f32_e32 v185, 0xbfb8aa3b, v0
	v_pk_fma_f32 v[188:189], v[52:53], v[188:189], v[54:55]
	v_mul_f32_e32 v51, v55, v201
	v_exp_f32_e32 v185, v185
	v_mul_f32_e32 v189, v188, v51
	ds_bpermute_b32 v2, v56, v189
	ds_bpermute_b32 v202, v57, v189
	ds_bpermute_b32 v3, v58, v189
	v_add_f32_e32 v185, 1.0, v185
	v_rcp_f32_e32 v185, v185
	v_pk_add_f32 v[190:191], v[182:183], 1.0 op_sel_hi:[1,0] neg_lo:[1,0] neg_hi:[1,0]
	s_waitcnt lgkmcnt(2)
	v_cndmask_b32_e64 v182, v2, 1.0, s[4:5]
	s_waitcnt lgkmcnt(1)
	v_cndmask_b32_e64 v194, 1.0, v202, s[6:7]
	v_mul_f32_e32 v182, v182, v194
	s_waitcnt lgkmcnt(0)
	v_cndmask_b32_e64 v194, 1.0, v3, s[8:9]
	v_mul_f32_e32 v194, v182, v194
	v_mul_f32_e32 v0, v185, v0
	v_mul_f32_e32 v182, v183, v194
	v_mul_f32_e32 v0, v0, v182
	v_add_u32_e32 v185, s57, v97
	ds_bpermute_b32 v203, v59, v189
	v_rcp_f32_e32 v183, v182
	v_cvt_pk_bf16_f32 v0, v0, s0
	ds_write_b16 v185, v0
	v_mul_f32_e32 v0, v184, v194
	v_rcp_f32_e32 v182, v0
	v_mul_f32_e32 v0, v208, v0
	v_mul_f32_e32 v184, v191, v183
	v_add_u32_e32 v209, s57, v125
	s_waitcnt lgkmcnt(1)
; #define LAS __attribute__((address_space(3)))
; __device__ __forceinline__ unsigned pk2(float a, float b) { f32x2 v = {a, b}; bf16x2_t r = __builtin_convertvector(v, bf16x2_t); return __builtin_bit_cast(unsigned, r); }
; __device__ __forceinline__ bf16_t f2bf(float a) { return (bf16_t)(pk2(a, 0.f) & 0xffffu); }
; __device__ __forceinline__ float frcp(float x) { return __builtin_amdgcn_rcpf(x); }
; __device__ __forceinline__ float silu(float x) { return x * frcp(1.f + __expf(-x)); }
; __device__ __forceinline__ bf16x8 pack8(const f32x4& a, const f32x4& b) { u32x4 w; w.x = pk2(a.x, a.y); w.y = pk2(a.z, a.w); w.z = pk2(b.x, b.y); w.w = pk2(b.z, b.w); return __builtin_bit_cast(bf16x8, w); }
; __device__ __forceinline__ void hgrn_mfma(const Params& p, LAS unsigned char* lds) {
;     ...
;             for (int i = 0; i < 8; ++i) {
;                 const int c = 8 * fq + i; const float E = pre * Pl[i], rE = frcp(E), k = 1.f - fv[i];
;                 *(LAS bf16_t*)(QG + rm_byte(c, d)) = f2bf(silu(qv[i]) * E);
;                 *(LAS bf16_t*)(KG + rm_byte(c, d)) = f2bf(k * rE);
;                 kd[i] = k * tot * rE;
;             }
;             { u32x4 wv; wv.x = pk2(kd[0], kd[1]); wv.y = pk2(kd[2], kd[3]); wv.z = pk2(kd[4], kd[5]); wv.w = pk2(kd[6], kd[7]);
;               *(LAS u32x4*)(KDT + d * 64 + ((fq ^ ((d >> 2) & 3)) << 4)) = wv; }
;             if (fq == 0) DEC[d] = tot;
;             const bf16x8 vB = pack8((f32x4){vv[0], vv[1], vv[2], vv[3]}, (f32x4){vv[4], vv[5], vv[6], vv[7]});
;             const bf16x8 vP = pack8((f32x4){vp[0], vp[1], vp[2], vp[3]}, (f32x4){vp[4], vp[5], vp[6], vp[7]});
;             __syncthreads();
;             f32x4 at00 = {0.f, 0.f, 0.f, 0.f}, at01 = at00, at11 = at00;
; #pragma unroll
;             for (int ks = 0; ks < 4; ++ks) {
;                 const int d0 = 32 * ks + 8 * fq;
;                 const bf16x8 kg0 = *(const LAS bf16x8*)(KG + rm_byte(fr, d0)), kg1 = *(const LAS bf16x8*)(KG + rm_byte(16 + fr, d0));
;                 const bf16x8 qg0 = *(const LAS bf16x8*)(QG + rm_byte(fr, d0)), qg1 = *(const LAS bf16x8*)(QG + rm_byte(16 + fr, d0));
;                 at00 = __builtin_amdgcn_mfma_f32_16x16x32_bf16(kg0, qg0, at00, 0, 0, 0);
;                 at01 = __builtin_amdgcn_mfma_f32_16x16x32_bf16(kg0, qg1, at01, 0, 0, 0);
;                 at11 = __builtin_amdgcn_mfma_f32_16x16x32_bf16(kg1, qg1, at11, 0, 0, 0);
	v_pk_mul_f32 v[2:3], v[2:3], v[202:203]
	v_cvt_pk_bf16_f32 v0, v0, s0
	v_cvt_pk_bf16_f32 v184, v184, s0
	v_pk_mul_f32 v[2:3], v[2:3], v[2:3] op_sel:[0,1] op_sel_hi:[1,0]
	ds_write_b16 v185, v184 offset:8192
	ds_write_b16 v209, v0 offset:256
	v_mul_f32_e32 v0, v190, v182
	v_pk_mul_f32 v[184:185], v[190:191], v[2:3] op_sel_hi:[1,0]
	v_cvt_pk_bf16_f32 v0, v0, s0
	v_pk_mul_f32 v[184:185], v[182:183], v[184:185]
	ds_write_b16 v209, v0 offset:8448
	v_mul_f32_e32 v0, v195, v194
	v_mul_f32_e32 v195, v197, v194
	v_pk_mov_b32 v[182:183], v[184:185], v[184:185] op_sel:[1,0]
	v_rcp_f32_e32 v184, v0
	v_rcp_f32_e32 v185, v195
	v_mul_f32_e32 v0, v210, v0
	v_pk_add_f32 v[190:191], v[192:193], 1.0 op_sel_hi:[1,0] neg_lo:[1,0] neg_hi:[1,0]
	v_add_u32_e32 v211, s57, v126
	v_cvt_pk_bf16_f32 v0, v0, s0
	v_pk_mul_f32 v[192:193], v[190:191], v[2:3] op_sel_hi:[1,0]
	ds_write_b16 v211, v0 offset:512
	v_mul_f32_e32 v0, v190, v184
	v_pk_mul_f32 v[192:193], v[184:185], v[192:193]
	v_mul_f32_e32 v184, 0xbfb8aa3b, v204
	v_cvt_pk_bf16_f32 v0, v0, s0
	v_exp_f32_e32 v184, v184
	ds_write_b16 v211, v0 offset:8704
	v_mul_f32_e32 v0, v212, v195
	v_add_u32_e32 v187, s57, v127
	v_cvt_pk_bf16_f32 v0, v0, s0
	ds_write_b16 v187, v0 offset:768
	v_mul_f32_e32 v0, v191, v185
	v_cvt_pk_bf16_f32 v0, v0, s0
	v_add_f32_e32 v184, 1.0, v184
	v_rcp_f32_e32 v185, v184
	ds_write_b16 v187, v0 offset:8960
	v_mul_f32_e32 v187, 0xbfb8aa3b, v205
	v_exp_f32_e32 v187, v187
	v_mul_f32_e32 v0, v198, v194
	v_mul_f32_e32 v185, v185, v204
	v_rcp_f32_e32 v184, v0
	v_mul_f32_e32 v0, v185, v0
	v_add_f32_e32 v185, 1.0, v187
	v_rcp_f32_e32 v187, v185
	v_cvt_pk_bf16_f32 v0, v0, s0
	v_add_u32_e32 v190, s57, v128
	ds_write_b16 v190, v0 offset:1024
	v_mul_f32_e32 v0, v201, v194
	v_mul_f32_e32 v187, v187, v205
	v_rcp_f32_e32 v185, v0
	v_mul_f32_e32 v0, v187, v0
	v_mov_b32_e32 v187, v53
	v_pk_add_f32 v[186:187], v[186:187], 1.0 op_sel_hi:[1,0] neg_lo:[1,0] neg_hi:[1,0]
	v_cvt_pk_bf16_f32 v0, v0, s0
	v_mul_f32_e32 v53, v186, v184
	v_cvt_pk_bf16_f32 v53, v53, s0
	ds_write_b16 v190, v53 offset:9216
	v_mul_f32_e32 v53, 0xbfb8aa3b, v206
	v_exp_f32_e32 v53, v53
	v_add_u32_e32 v195, s57, v129
	ds_write_b16 v195, v0 offset:1280
	v_mul_f32_e32 v0, v187, v185
	v_add_f32_e32 v53, 1.0, v53
	v_rcp_f32_e32 v53, v53
	v_cvt_pk_bf16_f32 v0, v0, s0
	ds_write_b16 v195, v0 offset:9472
	v_mul_f32_e32 v0, v51, v194
	v_mul_f32_e32 v51, v53, v206
	v_mul_f32_e32 v53, 0xbfb8aa3b, v207
	v_exp_f32_e32 v53, v53
	v_pk_mul_f32 v[190:191], v[186:187], v[2:3] op_sel_hi:[1,0]
	v_mov_b32_e32 v186, v55
	v_pk_mul_f32 v[190:191], v[184:185], v[190:191]
	v_add_f32_e32 v53, 1.0, v53
	v_rcp_f32_e32 v184, v0
	v_mul_f32_e32 v0, v51, v0
	v_rcp_f32_e32 v53, v53
	v_cvt_pk_bf16_f32 v0, v0, s0
	v_add_u32_e32 v51, s57, v130
	ds_write_b16 v51, v0 offset:1536
	v_mul_f32_e32 v0, v189, v194
	v_rcp_f32_e32 v185, v0
	v_mov_b32_e32 v187, v188
	v_mul_f32_e32 v53, v53, v207
	v_pk_add_f32 v[186:187], v[186:187], 1.0 op_sel_hi:[1,0] neg_lo:[1,0] neg_hi:[1,0]
	v_mul_f32_e32 v0, v53, v0
	v_mul_f32_e32 v55, v186, v184
	v_cvt_pk_bf16_f32 v0, v0, s0
	v_add_u32_e32 v53, s57, v131
	v_cvt_pk_bf16_f32 v55, v55, s0
	ds_write_b16 v51, v55 offset:9728
	v_pk_mul_f32 v[188:189], v[186:187], v[2:3] op_sel_hi:[1,0]
	ds_write_b16 v53, v0 offset:1792
	v_mul_f32_e32 v0, v187, v185
	v_pk_mul_f32 v[188:189], v[184:185], v[188:189]
	v_cvt_pk_bf16_f32 v0, v0, s0
	v_add_u32_e32 v3, s57, v60
	ds_write_b16 v53, v0 offset:9984
	v_cvt_pk_bf16_f32 v182, v182, v183
	v_cvt_pk_bf16_f32 v183, v192, v193
	v_cvt_pk_bf16_f32 v184, v190, v191
	v_cvt_pk_bf16_f32 v185, v188, v189
	v_add_u32_e32 v0, v3, v61
	ds_write_b128 v0, v[182:185] offset:16384
	s_and_saveexec_b64 s[46:47], s[4:5]
	v_add_u32_e32 v0, v3, v118
	ds_write_b32 v0, v2 offset:24576
	s_or_b64 exec, exec, s[46:47]
	v_add_u32_e32 v2, s57, v98
	s_waitcnt lgkmcnt(0)
	s_barrier
	ds_read_b128 v[182:185], v2 offset:8192
	v_lshlrev_b32_e32 v3, 16, v5
	v_add_u32_e32 v5, s57, v99
	ds_read_b128 v[186:189], v5 offset:8192
	ds_read_b128 v[190:193], v2
	ds_read_b128 v[194:197], v5
	v_add_u32_e32 v5, s57, v100
	ds_read_b128 v[198:201], v5 offset:8192
	v_add_u32_e32 v51, s57, v101
	ds_read_b128 v[202:205], v51 offset:8192
	ds_read_b128 v[206:209], v5
	v_add_u32_e32 v5, s57, v102
	s_waitcnt lgkmcnt(4)
	v_mfma_f32_16x16x32_bf16 v[190:193], v[182:185], v[190:193], 0
	ds_read_b128 v[210:213], v51
	ds_read_b128 v[214:217], v5 offset:8192
	v_add_u32_e32 v51, s57, v103
	s_waitcnt lgkmcnt(5)
	v_mfma_f32_16x16x32_bf16 v[186:189], v[186:189], v[194:197], 0
	v_lshlrev_b32_e32 v0, 16, v171
	v_lshlrev_b32_e32 v55, 16, v180
	s_waitcnt vmcnt(32)
	v_lshlrev_b32_e32 v171, 16, v181
	s_waitcnt lgkmcnt(2)
	v_mfma_f32_16x16x32_bf16 v[190:193], v[198:201], v[206:209], v[190:193]
	ds_read_b128 v[206:209], v51 offset:8192
	ds_read_b128 v[218:221], v5
	v_add_u32_e32 v5, s57, v104
	ds_read_b128 v[224:227], v5 offset:8192
	s_waitcnt lgkmcnt(4)
	v_mfma_f32_16x16x32_bf16 v[186:189], v[202:205], v[210:213], v[186:189]
	ds_read_b128 v[202:205], v51
	v_add_u32_e32 v51, s57, v105
	v_lshlrev_b32_e32 v2, 16, v175
	v_mfma_f32_16x16x32_bf16 v[180:183], v[182:185], v[194:197], 0
	v_lshlrev_b32_e32 v53, 16, v177
	s_add_i32 s56, s56, 1
	s_waitcnt lgkmcnt(2)
	v_mfma_f32_16x16x32_bf16 v[190:193], v[214:217], v[218:221], v[190:193]
	ds_read_b128 v[218:221], v51 offset:8192
	ds_read_b128 v[228:231], v5
	v_lshlrev_b32_e32 v5, 16, v172
	s_waitcnt lgkmcnt(2)
	v_mfma_f32_16x16x32_bf16 v[186:189], v[206:209], v[202:205], v[186:189]
	ds_read_b128 v[206:209], v51
	v_lshlrev_b32_e32 v51, 16, v176
	v_mfma_f32_16x16x32_bf16 v[180:183], v[198:201], v[210:213], v[180:183]
	s_waitcnt lgkmcnt(1)
; #define LAS __attribute__((address_space(3)))
; __device__ __forceinline__ void hgrn_mfma(const Params& p, LAS unsigned char* lds) {
;     ...
; #pragma unroll
;             for (int j = 0; j < 4; ++j) { const bool ok = (4 * fq + j) <= fr; at00[j] = ok ? at00[j] : 0.f; at11[j] = ok ? at11[j] : 0.f; }
;             const bf16x8 bi0 = pack8(at00, (f32x4){0.f, 0.f, 0.f, 0.f}), bi1 = pack8(at01, at11);
;             f32x4 o0 = {0.f, 0.f, 0.f, 0.f}, o1 = o0;
;             o0 = __builtin_amdgcn_mfma_f32_16x16x32_bf16(vP, bi0, o0, 0, 0, 0);
;             o1 = __builtin_amdgcn_mfma_f32_16x16x32_bf16(vP, bi1, o1, 0, 0, 0);
; #pragma unroll
;             for (int ks = 0; ks < 4; ++ks) {
;                 const bf16x8 sb = pack8(S[2 * ks], S[2 * ks + 1]);
;                 const int da = 32 * ks + 4 * fq, db = da + 16;
;                 const bf16x4 q0a = *(const LAS bf16x4*)(QG + rm_byte(fr, da)), q0b = *(const LAS bf16x4*)(QG + rm_byte(fr, db));
;                 const bf16x4 q1a = *(const LAS bf16x4*)(QG + rm_byte(16 + fr, da)), q1b = *(const LAS bf16x4*)(QG + rm_byte(16 + fr, db));
;                 const bf16x8 qp0 = {q0a[0], q0a[1], q0a[2], q0a[3], q0b[0], q0b[1], q0b[2], q0b[3]}, qp1 = {q1a[0], q1a[1], q1a[2], q1a[3], q1b[0], q1b[1], q1b[2], q1b[3]};
;                 o0 = __builtin_amdgcn_mfma_f32_16x16x32_bf16(sb, qp0, o0, 0, 0, 0);
;                 o1 = __builtin_amdgcn_mfma_f32_16x16x32_bf16(sb, qp1, o1, 0, 0, 0);
;             }
;             { const int c0 = fr, c1 = 16 + fr; const int t0 = dir ? (T - 1 - (32 * n + c0)) : (32 * n + c0), t1 = dir ? (T - 1 - (32 * n + c1)) : (32 * n + c1);
;               bf16_t* ob = oscr + ((size_t)dir * M + (size_t)b * T) * 1024 + h * 128 + 16 * w + 4 * fq;
;               u32x2 w0; w0.x = pk2(o0[0], o0[1]); w0.y = pk2(o0[2], o0[3]); u32x2 w1; w1.x = pk2(o1[0], o1[1]); w1.y = pk2(o1[2], o1[3]);
;               *(u32x2*)(ob + (size_t)t0 * 1024) = w0; *(u32x2*)(ob + (size_t)t1 * 1024) = w1; }
; #pragma unroll
;             for (int mi = 0; mi < 8; ++mi) {
;                 const int dr = 16 * mi + fr;
;                 const bf16x8 ka = *(const LAS bf16x8*)(KDT + dr * 64 + ((fq ^ ((dr >> 2) & 3)) << 4));
;                 const f32x4 dc = *(const LAS f32x4*)(DEC + 16 * mi + 4 * fq);
;                 S[mi] = __builtin_amdgcn_mfma_f32_16x16x32_bf16(ka, vB, S[mi] * dc, 0, 0, 0);
	v_mfma_f32_16x16x32_bf16 v[190:193], v[224:227], v[228:231], v[190:193]
	v_mfma_f32_16x16x32_bf16 v[180:183], v[214:217], v[202:205], v[180:183]
	s_waitcnt lgkmcnt(0)
	v_mfma_f32_16x16x32_bf16 v[186:189], v[218:221], v[206:209], v[186:189]
	v_cvt_pk_bf16_f32 v218, v0, v3
	v_cvt_pk_bf16_f32 v219, v2, v5
	v_cvt_pk_bf16_f32 v220, v53, v51
	v_cvt_pk_bf16_f32 v221, v55, v171
	s_nop 0
	v_cndmask_b32_e64 v0, v190, 0, s[10:11]
	v_cndmask_b32_e64 v2, 0, v191, s[12:13]
	v_cndmask_b32_e64 v3, v192, 0, s[14:15]
	v_cndmask_b32_e64 v5, v193, 0, s[16:17]
	v_mfma_f32_16x16x32_bf16 v[180:183], v[224:227], v[206:209], v[180:183]
	v_cvt_pk_bf16_f32 v2, v0, v2
	v_cvt_pk_bf16_f32 v3, v3, v5
	v_mov_b32_e32 v5, v4
	v_add_u32_e32 v0, s57, v62
	v_cndmask_b32_e64 v51, v186, 0, s[10:11]
	v_cndmask_b32_e64 v53, 0, v187, s[12:13]
	v_mfma_f32_16x16x32_bf16 v[184:187], v[218:221], v[2:5], 0
	v_add_u32_e32 v2, s57, v63
	v_add_u32_e32 v3, v0, v106
	v_cndmask_b32_e64 v55, v188, 0, s[14:15]
	v_cndmask_b32_e64 v171, v189, 0, s[16:17]
	v_add_u32_e32 v5, v0, v107
	ds_read_b64 v[192:193], v3
	ds_read_b64 v[194:195], v5
	v_add_u32_e32 v3, v2, v106
	v_cvt_pk_bf16_f32 v180, v180, v181
	v_cvt_pk_bf16_f32 v181, v182, v183
	v_cvt_pk_bf16_f32 v182, v51, v53
	v_cvt_pk_bf16_f32 v183, v55, v171
	v_cvt_pk_bf16_f32 v188, v34, v35
	v_cvt_pk_bf16_f32 v189, v36, v37
	v_cvt_pk_bf16_f32 v190, v30, v31
	v_cvt_pk_bf16_f32 v191, v32, v33
	v_add_u32_e32 v5, v2, v107
	ds_read_b64 v[196:197], v3
	ds_read_b64 v[198:199], v5
	v_mfma_f32_16x16x32_bf16 v[180:183], v[218:221], v[180:183], 0
	v_add_u32_e32 v53, v0, v108
	v_add_u32_e32 v55, v0, v109
	v_lshlrev_b32_e32 v5, 16, v160
	s_waitcnt lgkmcnt(2)
	v_mfma_f32_16x16x32_bf16 v[184:187], v[188:191], v[192:195], v[184:187]
	ds_read_b64 v[192:193], v53
	ds_read_b64 v[194:195], v55
	v_add_u32_e32 v53, v2, v108
	v_add_u32_e32 v55, v2, v109
	s_waitcnt lgkmcnt(2)
	v_mfma_f32_16x16x32_bf16 v[180:183], v[188:191], v[196:199], v[180:183]
	v_cvt_pk_bf16_f32 v188, v26, v27
	v_cvt_pk_bf16_f32 v189, v28, v29
	v_cvt_pk_bf16_f32 v190, v22, v23
	v_cvt_pk_bf16_f32 v191, v24, v25
	ds_read_b64 v[196:197], v53
	ds_read_b64 v[198:199], v55
	v_add_u32_e32 v160, v0, v110
	s_waitcnt lgkmcnt(2)
	v_mfma_f32_16x16x32_bf16 v[184:187], v[188:191], v[192:195], v[184:187]
	v_lshlrev_b32_e32 v53, 16, v161
	v_add_u32_e32 v161, v0, v111
	ds_read_b64 v[192:193], v160
	ds_read_b64 v[194:195], v161
	v_add_u32_e32 v160, v2, v110
	s_waitcnt lgkmcnt(2)
	v_mfma_f32_16x16x32_bf16 v[180:183], v[188:191], v[196:199], v[180:183]
	v_cvt_pk_bf16_f32 v188, v18, v19
	v_cvt_pk_bf16_f32 v189, v20, v21
	v_cvt_pk_bf16_f32 v190, v10, v11
	v_cvt_pk_bf16_f32 v191, v12, v13
	v_add_u32_e32 v161, v2, v111
	ds_read_b64 v[196:197], v160
	ds_read_b64 v[198:199], v161
	v_lshlrev_b32_e32 v3, 16, v159
	v_cvt_pk_bf16_f32 v160, v3, v5
	v_add_u32_e32 v3, v0, v112
	v_lshlrev_b32_e32 v51, 16, v165
	v_lshlrev_b32_e32 v55, 16, v163
	v_lshlrev_b32_e32 v159, 16, v166
	s_waitcnt lgkmcnt(2)
	v_mfma_f32_16x16x32_bf16 v[184:187], v[188:191], v[192:195], v[184:187]
	v_lshlrev_b32_e32 v166, 16, v162
	v_lshlrev_b32_e32 v171, 16, v164
	v_add_u32_e32 v0, v0, v113
	s_waitcnt lgkmcnt(0)
	v_mfma_f32_16x16x32_bf16 v[180:183], v[188:191], v[196:199], v[180:183]
	v_cvt_pk_bf16_f32 v188, v6, v7
	v_cvt_pk_bf16_f32 v189, v8, v9
	v_cvt_pk_bf16_f32 v190, v14, v15
	v_cvt_pk_bf16_f32 v191, v16, v17
	ds_read_b64 v[162:163], v3
	ds_read_b64 v[164:165], v0
	v_add_u32_e32 v0, v2, v112
	v_add_u32_e32 v2, v2, v113
	ds_read_b64 v[192:193], v0
	ds_read_b64 v[194:195], v2
	s_waitcnt lgkmcnt(2)
	v_mfma_f32_16x16x32_bf16 v[184:187], v[188:191], v[162:165], v[184:187]
	v_add_u32_e32 v0, s54, v64
	v_add_u32_e32 v3, s55, v1
	v_cndmask_b32_e64 v2, v0, v3, s[18:19]
	v_add_u32_e32 v0, s54, v65
	v_add_u32_e32 v3, 16, v3
	s_waitcnt lgkmcnt(0)
	v_mfma_f32_16x16x32_bf16 v[180:183], v[188:191], v[192:195], v[180:183]
	v_cndmask_b32_e64 v164, v0, v3, s[18:19]
	v_ashrrev_i32_e32 v3, 31, v2
	v_lshlrev_b64 v[2:3], 11, v[2:3]
	v_cvt_pk_bf16_f32 v176, v184, v185
	v_cvt_pk_bf16_f32 v177, v186, v187
	v_lshl_add_u64 v[2:3], v[42:43], 0, v[2:3]
	v_add_u32_e32 v0, s57, v61
	v_cvt_pk_bf16_f32 v161, v51, v53
	v_mov_b64_e32 v[248:249], v[2:3]
	v_mov_b64_e32 v[250:251], v[176:177]
	v_lshl_add_u32 v5, v40, 2, s57
	v_add_u32_e32 v53, v0, v114
	v_cvt_pk_bf16_f32 v204, v180, v181
	v_cvt_pk_bf16_f32 v205, v182, v183
	v_add_u32_e32 v51, v0, v96
	ds_read_b128 v[180:183], v5 offset:24576
	ds_read_b128 v[184:187], v51 offset:16384
	ds_read_b128 v[192:195], v53 offset:16384
	ds_read_b128 v[188:191], v5 offset:24640
	v_cvt_pk_bf16_f32 v162, v55, v159
	v_cvt_pk_bf16_f32 v163, v166, v171
	s_waitcnt lgkmcnt(3)
	v_pk_mul_f32 v[36:37], v[36:37], v[182:183]
	v_pk_mul_f32 v[34:35], v[34:35], v[180:181]
	ds_read_b128 v[180:183], v51 offset:20480
	s_waitcnt lgkmcnt(1)
	v_pk_mul_f32 v[32:33], v[32:33], v[190:191]
	v_pk_mul_f32 v[30:31], v[30:31], v[188:189]
	v_add_u32_e32 v53, v0, v115
	v_mfma_f32_16x16x32_bf16 v[34:37], v[184:187], v[160:163], v[34:37]
	ds_read_b128 v[184:187], v53 offset:16384
	ds_read_b128 v[188:191], v51 offset:23552
	v_add_u32_e32 v0, v0, v116
	v_ashrrev_i32_e32 v165, 31, v164
	v_mfma_f32_16x16x32_bf16 v[30:33], v[192:195], v[160:163], v[30:33]
	ds_read_b128 v[192:195], v5 offset:24704
	ds_read_b128 v[196:199], v0 offset:16384
	ds_read_b128 v[200:203], v5 offset:24768
	v_lshlrev_b64 v[2:3], 11, v[164:165]
	s_add_i32 s55, s55, 32
	s_sub_i32 s54, s54, 32
	s_waitcnt lgkmcnt(2)
	v_pk_mul_f32 v[28:29], v[28:29], v[194:195]
	v_pk_mul_f32 v[26:27], v[26:27], v[192:193]
	s_waitcnt lgkmcnt(0)
	v_pk_mul_f32 v[24:25], v[24:25], v[202:203]
	v_pk_mul_f32 v[22:23], v[22:23], v[200:201]
	v_mfma_f32_16x16x32_bf16 v[26:29], v[184:187], v[160:163], v[26:29]
	ds_read_b128 v[184:187], v5 offset:24832
	v_lshl_add_u64 v[2:3], v[42:43], 0, v[2:3]
	s_cmpk_eq_i32 s55, 0x7e0
	v_mfma_f32_16x16x32_bf16 v[22:25], v[196:199], v[160:163], v[22:25]
	ds_read_b128 v[192:195], v51 offset:21504
	ds_read_b128 v[196:199], v5 offset:24896
	s_waitcnt lgkmcnt(2)
	v_pk_mul_f32 v[20:21], v[20:21], v[186:187]
	v_pk_mul_f32 v[18:19], v[18:19], v[184:185]
	ds_read_b128 v[184:187], v5 offset:24960
	v_mov_b64_e32 v[252:253], v[2:3]
	v_mov_b64_e32 v[132:133], v[204:205]
	v_mfma_f32_16x16x32_bf16 v[18:21], v[180:183], v[160:163], v[18:21]
	ds_read_b128 v[180:183], v51 offset:22528
	s_waitcnt lgkmcnt(2)
	v_pk_mul_f32 v[12:13], v[12:13], v[198:199]
	v_pk_mul_f32 v[10:11], v[10:11], v[196:197]
	s_nop 1
	v_mfma_f32_16x16x32_bf16 v[10:13], v[192:195], v[160:163], v[10:13]
	ds_read_b128 v[192:195], v5 offset:25024
	s_waitcnt lgkmcnt(2)
	v_pk_mul_f32 v[8:9], v[8:9], v[186:187]
	v_pk_mul_f32 v[6:7], v[6:7], v[184:185]
	s_waitcnt lgkmcnt(0)
	v_pk_mul_f32 v[16:17], v[16:17], v[194:195]
	v_pk_mul_f32 v[14:15], v[14:15], v[192:193]
	v_mfma_f32_16x16x32_bf16 v[6:9], v[180:183], v[160:163], v[6:9]
	s_nop 0
	v_mfma_f32_16x16x32_bf16 v[14:17], v[188:191], v[160:163], v[14:17]
	s_cbranch_scc1 .LBB0_279
; #define LAS __attribute__((address_space(3)))
; __device__ __forceinline__ float bf2f(bf16_t v) { return __uint_as_float((unsigned)v << 16); }
; __device__ __forceinline__ bf16_t f2bf(float a) { return (bf16_t)(pk2(a, 0.f) & 0xffffu); }
; __device__ __forceinline__ float frcp(float x) { return __builtin_amdgcn_rcpf(x); }
; __device__ __forceinline__ float sigm(float x) { return frcp(1.f + __expf(-x)); }
; __device__ __forceinline__ float silu(float x) { return x * frcp(1.f + __expf(-x)); }
; __device__ __forceinline__ void hgrn_mfma(const Params& p, LAS unsigned char* lds) {
;     ...
;             float qv[8], fv[8], vv[8], vp[8];
; #pragma unroll
;             for (int i = 0; i < 8; ++i) { qv[i] = bf2f(rq[i]); vv[i] = bf2f(rv[i]); fv[i] = bf2f(rz[i]); vp[i] = bf2f(rp[i]); }
;             if (n + 1 < T / 32) HG_LOAD(n + 1);
;             float Pl[8]; float P = 1.f;
; #pragma unroll
;             for (int i = 0; i < 8; ++i) { fv[i] = lb + (1.f - lb) * sigm(fv[i]); P *= fv[i]; Pl[i] = P; }
;             const float p0 = __shfl(P, fr), p1 = __shfl(P, fr + 16), p2 = __shfl(P, fr + 32), p3 = __shfl(P, fr + 48);
;             const float pre = (fq > 0 ? p0 : 1.f) * (fq > 1 ? p1 : 1.f) * (fq > 2 ? p2 : 1.f), tot = (p0 * p1) * (p2 * p3);
;             float kd[8];
; #pragma unroll
;             for (int i = 0; i < 8; ++i) {
;                 const int c = 8 * fq + i; const float E = pre * Pl[i], rE = frcp(E), k = 1.f - fv[i];
;                 *(LAS bf16_t*)(QG + rm_byte(c, d)) = f2bf(silu(qv[i]) * E);
	s_waitcnt vmcnt(4)
	v_mov_b32_e32 v164, v179
	v_mov_b32_e32 v162, v178
	v_mov_b32_e32 v166, v174
	v_mov_b32_e32 v163, v173
	v_mov_b32_e32 v161, v170
	v_mov_b32_e32 v165, v169
	v_mov_b32_e32 v160, v168
	v_mov_b32_e32 v159, v167
	s_waitcnt vmcnt(2)
	v_mov_b32_e32 v181, v152
	v_mov_b32_e32 v180, v150
	v_mov_b32_e32 v176, v148
	v_mov_b32_e32 v177, v147
	v_mov_b32_e32 v172, v142
	v_mov_b32_e32 v175, v146
	v_mov_b32_e32 v5, v140
	v_mov_b32_e32 v171, v143
	s_branch .LBB0_275
.LBB0_279:
	global_store_dwordx2 v[248:249], v[250:251], off
	global_store_dwordx2 v[252:253], v[132:133], off
	s_waitcnt vmcnt(11)
	v_lshlrev_b32_e32 v53, 16, v154
	v_mul_f32_e32 v53, 0xbfb8aa3b, v53
	v_exp_f32_e32 v53, v53
	v_lshlrev_b32_e32 v151, 16, v151
	v_lshlrev_b32_e32 v2, 16, v138
	v_lshlrev_b32_e32 v138, 16, v136
	v_mul_f32_e32 v136, 0xbfb8aa3b, v151
	v_exp_f32_e32 v136, v136
	v_add_f32_e32 v53, 1.0, v53
	v_lshlrev_b32_e32 v3, 16, v137
	v_rcp_f32_e32 v137, v53
	s_waitcnt vmcnt(7)
	v_lshlrev_b32_e32 v51, 16, v156
	v_mul_f32_e32 v51, 0xbfb8aa3b, v51
	v_lshlrev_b32_e32 v55, 16, v141
	v_lshlrev_b32_e32 v141, 16, v139
	v_lshlrev_b32_e32 v135, 16, v135
	v_exp_f32_e32 v139, v51
	v_add_f32_e32 v51, 1.0, v136
	v_mul_f32_e32 v3, 0xbfb8aa3b, v3
	v_mul_f32_e32 v2, 0xbfb8aa3b, v2
	v_rcp_f32_e32 v53, v51
	v_fma_f32 v51, v52, v137, v50
	v_mul_f32_e32 v137, 0xbfb8aa3b, v135
	v_exp_f32_e32 v3, v3
	v_exp_f32_e32 v44, v2
	v_exp_f32_e32 v137, v137
	s_waitcnt vmcnt(3)
	v_lshlrev_b32_e32 v0, 16, v158
	v_mul_f32_e32 v0, 0xbfb8aa3b, v0
	v_add_f32_e32 v2, 1.0, v3
	v_add_f32_e32 v3, 1.0, v44
	v_exp_f32_e32 v0, v0
	v_add_f32_e32 v137, 1.0, v137
	v_rcp_f32_e32 v2, v2
	v_rcp_f32_e32 v3, v3
	v_add_f32_e32 v136, 1.0, v139
	v_rcp_f32_e32 v139, v137
	v_mul_f32_e32 v137, 0xbfb8aa3b, v138
	v_lshlrev_b32_e32 v54, 16, v145
	v_exp_f32_e32 v145, v137
	v_add_f32_e32 v0, 1.0, v0
	v_lshlrev_b32_e32 v144, 16, v144
	v_pk_fma_f32 v[44:45], v[48:49], v[2:3], v[46:47]
	v_mul_f32_e32 v2, 0xbfb8aa3b, v55
	v_mul_f32_e32 v3, 0xbfb8aa3b, v54
	v_rcp_f32_e32 v137, v0
	v_mul_f32_e32 v0, v139, v135
	v_mul_f32_e32 v139, 0xbfb8aa3b, v141
	v_exp_f32_e32 v2, v2
	v_exp_f32_e32 v3, v3
	v_add_f32_e32 v135, 1.0, v145
	v_exp_f32_e32 v139, v139
	v_mul_f32_e32 v145, 0xbfb8aa3b, v144
	v_exp_f32_e32 v145, v145
	v_add_f32_e32 v2, 1.0, v2
	v_add_f32_e32 v3, 1.0, v3
	v_add_f32_e32 v139, 1.0, v139
	v_rcp_f32_e32 v2, v2
	v_rcp_f32_e32 v3, v3
	v_rcp_f32_e32 v151, v139
	v_add_f32_e32 v139, 1.0, v145
	v_rcp_f32_e32 v145, v139
	v_pk_mul_f32 v[54:55], v[44:45], v[44:45] op_sel:[0,1] op_sel_hi:[1,0]
	v_pk_fma_f32 v[2:3], v[48:49], v[2:3], v[46:47]
	v_lshlrev_b32_e32 v5, 16, v157
	v_lshlrev_b32_e32 v158, 16, v155
	v_mul_f32_e32 v141, v151, v141
	v_mul_f32_e32 v151, v145, v144
	v_mov_b32_e32 v144, v54
	v_mov_b32_e32 v145, v52
	v_mov_b32_e32 v52, v2
	v_mov_b32_e32 v156, v3
	v_mov_b32_e32 v157, v50
	v_pk_fma_f32 v[52:53], v[144:145], v[52:53], v[156:157]
	v_mul_f32_e32 v144, 0xbfb8aa3b, v158
	v_exp_f32_e32 v156, v144
	v_pk_mul_f32 v[154:155], v[54:55], v[2:3]
	v_rcp_f32_e32 v135, v135
	v_mul_f32_e32 v52, v154, v3
	v_pk_add_f32 v[144:145], v[2:3], 1.0 op_sel_hi:[1,0] neg_lo:[1,0] neg_hi:[1,0]
	v_add_f32_e32 v2, 1.0, v156
	v_mul_f32_e32 v3, 0xbfb8aa3b, v5
	v_rcp_f32_e32 v2, v2
	v_exp_f32_e32 v3, v3
	v_rcp_f32_e32 v136, v136
	v_lshlrev_b32_e32 v153, 16, v153
	v_lshlrev_b32_e32 v149, 16, v149
	v_mul_f32_e32 v135, v135, v138
	v_pk_add_f32 v[138:139], v[44:45], 1.0 op_sel_hi:[1,0] neg_lo:[1,0] neg_hi:[1,0]
	v_mul_f32_e32 v45, 0xbfb8aa3b, v149
	v_mul_f32_e32 v50, 0xbfb8aa3b, v153
	v_mul_f32_e32 v55, v52, v53
	v_exp_f32_e32 v45, v45
	v_exp_f32_e32 v50, v50
	v_mul_f32_e32 v156, v2, v158
	v_add_f32_e32 v2, 1.0, v3
	v_mul_f32_e32 v155, v55, v51
	v_rcp_f32_e32 v3, v2
	v_pk_fma_f32 v[46:47], v[48:49], v[136:137], v[46:47]
	v_add_f32_e32 v45, 1.0, v45
	v_mul_f32_e32 v136, v155, v46
	v_mul_f32_e32 v137, v136, v47
	v_add_f32_e32 v50, 1.0, v50
	ds_bpermute_b32 v2, v56, v137
	ds_bpermute_b32 v48, v57, v137
	v_rcp_f32_e32 v45, v45
	v_rcp_f32_e32 v50, v50
	v_mul_f32_e32 v5, v3, v5
	ds_bpermute_b32 v3, v58, v137
	v_mul_f32_e32 v149, v45, v149
	v_mul_f32_e32 v153, v50, v153
	v_mov_b32_e32 v50, v53
	ds_bpermute_b32 v49, v59, v137
	s_waitcnt lgkmcnt(3)
; #define LAS __attribute__((address_space(3)))
; __device__ __forceinline__ unsigned pk2(float a, float b) { f32x2 v = {a, b}; bf16x2_t r = __builtin_convertvector(v, bf16x2_t); return __builtin_bit_cast(unsigned, r); }
; __device__ __forceinline__ bf16_t f2bf(float a) { return (bf16_t)(pk2(a, 0.f) & 0xffffu); }
; __device__ __forceinline__ float frcp(float x) { return __builtin_amdgcn_rcpf(x); }
; __device__ __forceinline__ float sigm(float x) { return frcp(1.f + __expf(-x)); }
; __device__ __forceinline__ float silu(float x) { return x * frcp(1.f + __expf(-x)); }
; __device__ __forceinline__ void hgrn_mfma(const Params& p, LAS unsigned char* lds) {
;     ...
;             for (int i = 0; i < 8; ++i) { fv[i] = lb + (1.f - lb) * sigm(fv[i]); P *= fv[i]; Pl[i] = P; }
;             const float p0 = __shfl(P, fr), p1 = __shfl(P, fr + 16), p2 = __shfl(P, fr + 32), p3 = __shfl(P, fr + 48);
;             const float pre = (fq > 0 ? p0 : 1.f) * (fq > 1 ? p1 : 1.f) * (fq > 2 ? p2 : 1.f), tot = (p0 * p1) * (p2 * p3);
;             float kd[8];
; #pragma unroll
;             for (int i = 0; i < 8; ++i) {
;                 const int c = 8 * fq + i; const float E = pre * Pl[i], rE = frcp(E), k = 1.f - fv[i];
;                 *(LAS bf16_t*)(QG + rm_byte(c, d)) = f2bf(silu(qv[i]) * E);
;                 *(LAS bf16_t*)(KG + rm_byte(c, d)) = f2bf(k * rE);
;                 kd[i] = k * tot * rE;
;             }
;             { u32x4 wv; wv.x = pk2(kd[0], kd[1]); wv.y = pk2(kd[2], kd[3]); wv.z = pk2(kd[4], kd[5]); wv.w = pk2(kd[6], kd[7]);
;               *(LAS u32x4*)(KDT + d * 64 + ((fq ^ ((d >> 2) & 3)) << 4)) = wv; }
;             if (fq == 0) DEC[d] = tot;
	v_cndmask_b32_e64 v45, v2, 1.0, s[4:5]
	s_waitcnt lgkmcnt(2)
	v_cndmask_b32_e64 v53, 1.0, v48, s[6:7]
	v_mul_f32_e32 v45, v45, v53
	s_waitcnt lgkmcnt(1)
	v_cndmask_b32_e64 v53, 1.0, v3, s[8:9]
	v_mul_f32_e32 v157, v45, v53
	v_mul_f32_e32 v45, v44, v157
	v_rcp_f32_e32 v44, v45
	v_mul_f32_e32 v0, v0, v45
	s_waitcnt lgkmcnt(0)
	v_pk_mul_f32 v[2:3], v[2:3], v[48:49]
	v_cvt_pk_bf16_f32 v0, v0, s0
	v_add_u32_e32 v48, 0, v97
	ds_write_b16 v48, v0 offset:25088
	v_mul_f32_e32 v0, v54, v157
	v_rcp_f32_e32 v45, v0
	v_mul_f32_e32 v49, v138, v44
	v_pk_mul_f32 v[2:3], v[2:3], v[2:3] op_sel:[0,1] op_sel_hi:[1,0]
	v_cvt_pk_bf16_f32 v49, v49, s0
	v_mul_f32_e32 v0, v135, v0
	ds_write_b16 v48, v49 offset:33280
	v_pk_mul_f32 v[48:49], v[138:139], v[2:3] op_sel_hi:[1,0]
	v_cvt_pk_bf16_f32 v0, v0, s0
	v_pk_mul_f32 v[48:49], v[44:45], v[48:49]
	v_add_u32_e32 v44, 0, v125
	ds_write_b16 v44, v0 offset:25344
	v_mul_f32_e32 v0, v139, v45
	v_cvt_pk_bf16_f32 v0, v0, s0
	ds_write_b16 v44, v0 offset:33536
	v_mul_f32_e32 v0, v154, v157
	v_rcp_f32_e32 v44, v0
	v_mul_f32_e32 v0, v141, v0
	v_mul_f32_e32 v54, v52, v157
	v_cvt_pk_bf16_f32 v0, v0, s0
	v_add_u32_e32 v53, 0, v126
	v_rcp_f32_e32 v45, v54
	ds_write_b16 v53, v0 offset:25600
	v_mul_f32_e32 v0, v144, v44
	v_cvt_pk_bf16_f32 v0, v0, s0
	ds_write_b16 v53, v0 offset:33792
	v_pk_mul_f32 v[52:53], v[144:145], v[2:3] op_sel_hi:[1,0]
	v_mul_f32_e32 v0, v151, v54
	v_pk_mul_f32 v[52:53], v[44:45], v[52:53]
	v_cvt_pk_bf16_f32 v0, v0, s0
	v_add_u32_e32 v44, 0, v127
	ds_write_b16 v44, v0 offset:25856
	v_mul_f32_e32 v0, v145, v45
	v_cvt_pk_bf16_f32 v0, v0, s0
	ds_write_b16 v44, v0 offset:34048
	v_mul_f32_e32 v0, v55, v157
	v_rcp_f32_e32 v44, v0
	v_mul_f32_e32 v0, v149, v0
	v_cvt_pk_bf16_f32 v0, v0, s0
	v_add_u32_e32 v54, 0, v128
	ds_write_b16 v54, v0 offset:26112
	v_mul_f32_e32 v0, v155, v157
	v_pk_add_f32 v[50:51], v[50:51], 1.0 op_sel_hi:[1,0] neg_lo:[1,0] neg_hi:[1,0]
	v_rcp_f32_e32 v45, v0
	v_mul_f32_e32 v55, v50, v44
	v_cvt_pk_bf16_f32 v55, v55, s0
	v_mul_f32_e32 v0, v153, v0
	ds_write_b16 v54, v55 offset:34304
	v_pk_mul_f32 v[54:55], v[50:51], v[2:3] op_sel_hi:[1,0]
	v_cvt_pk_bf16_f32 v0, v0, s0
	v_pk_mul_f32 v[54:55], v[44:45], v[54:55]
	v_add_u32_e32 v44, 0, v129
	ds_write_b16 v44, v0 offset:26368
	v_mul_f32_e32 v0, v51, v45
	v_cvt_pk_bf16_f32 v0, v0, s0
	ds_write_b16 v44, v0 offset:34560
	v_mul_f32_e32 v0, v136, v157
	v_rcp_f32_e32 v44, v0
	v_mul_f32_e32 v0, v156, v0
	v_cvt_pk_bf16_f32 v0, v0, s0
	v_add_u32_e32 v50, 0, v130
	v_pk_add_f32 v[46:47], v[46:47], 1.0 op_sel_hi:[1,0] neg_lo:[1,0] neg_hi:[1,0]
	v_mul_f32_e32 v135, v137, v157
	ds_write_b16 v50, v0 offset:26624
	v_mul_f32_e32 v0, v46, v44
	v_rcp_f32_e32 v45, v135
	v_cvt_pk_bf16_f32 v0, v0, s0
	ds_write_b16 v50, v0 offset:34816
	v_mul_f32_e32 v0, v5, v135
	v_pk_mul_f32 v[50:51], v[46:47], v[2:3] op_sel_hi:[1,0]
	v_cvt_pk_bf16_f32 v0, v0, s0
	v_add_u32_e32 v3, 0, v131
	ds_write_b16 v3, v0 offset:26880
	v_mul_f32_e32 v0, v47, v45
	v_pk_mul_f32 v[50:51], v[44:45], v[50:51]
	v_cvt_pk_bf16_f32 v0, v0, s0
	ds_write_b16 v3, v0 offset:35072
	v_cvt_pk_bf16_f32 v44, v48, v49
	v_cvt_pk_bf16_f32 v45, v52, v53
	v_cvt_pk_bf16_f32 v46, v54, v55
	v_cvt_pk_bf16_f32 v47, v50, v51
	v_add_u32_e32 v0, v117, v61
	ds_write_b128 v0, v[44:47] offset:41472
	s_and_saveexec_b64 s[46:47], s[4:5]
	s_cbranch_execz .LBB0_273
	v_add_u32_e32 v0, v117, v118
	ds_write_b32 v0, v2 offset:49664
	s_branch .LBB0_273
